# placement: indexer head loop at offset 48 mod 64 (pads only; other loops unchanged)
# baseline (speedup 1.0000x reference)
; #define LAS __attribute__((address_space(3)))
; __global__ void __launch_bounds__(NTHREADS, 2) mega_fwd(Args args) {
;     ...
;             if (act) {
;                 LAS unsigned char* Qs = F.lds + buf * 65536; LAS float* Ws = Wsb + buf * 512;
;                 f32x16 sacc[4];
; #pragma unroll
;                 for (int j = 0; j < 4; ++j) sacc[j] = f32x16{};
; #pragma unroll 2
;                 for (int h = 0; h < NIH; ++h) {
.LBB0_655:
	v_mov_b32_e32 v206, 0
	v_lshl_add_u32 v233, s25, 16, v230
	v_lshl_add_u32 v234, s25, 11, v231
	s_mov_b32 s7, 0
	v_mov_b32_e32 v207, v206
	v_mov_b32_e32 v208, v206
	v_mov_b32_e32 v209, v206
	v_mov_b32_e32 v210, v206
	v_mov_b32_e32 v211, v206
	v_mov_b32_e32 v212, v206
	v_mov_b32_e32 v213, v206
	v_mov_b32_e32 v214, v206
	v_mov_b32_e32 v215, v206
	v_mov_b32_e32 v216, v206
	v_mov_b32_e32 v217, v206
	v_mov_b32_e32 v218, v206
	v_mov_b32_e32 v219, v206
	v_mov_b32_e32 v220, v206
	v_mov_b32_e32 v221, v206
	v_mov_b32_e32 v190, v206
	v_mov_b32_e32 v191, v206
	v_mov_b32_e32 v192, v206
	v_mov_b32_e32 v193, v206
	v_mov_b32_e32 v194, v206
	v_mov_b32_e32 v195, v206
	v_mov_b32_e32 v196, v206
	v_mov_b32_e32 v197, v206
	v_mov_b32_e32 v198, v206
	v_mov_b32_e32 v199, v206
	v_mov_b32_e32 v200, v206
	v_mov_b32_e32 v201, v206
	v_mov_b32_e32 v202, v206
	v_mov_b32_e32 v203, v206
	v_mov_b32_e32 v204, v206
	v_mov_b32_e32 v205, v206
	v_mov_b32_e32 v188, v206
	v_mov_b32_e32 v189, v206
	v_mov_b32_e32 v186, v206
	v_mov_b32_e32 v187, v206
	v_mov_b32_e32 v184, v206
	v_mov_b32_e32 v185, v206
	v_mov_b32_e32 v182, v206
	v_mov_b32_e32 v183, v206
	v_mov_b32_e32 v180, v206
	v_mov_b32_e32 v181, v206
	v_mov_b32_e32 v178, v206
	v_mov_b32_e32 v179, v206
	v_mov_b32_e32 v176, v206
	v_mov_b32_e32 v177, v206
	v_mov_b32_e32 v174, v206
	v_mov_b32_e32 v175, v206
	v_mov_b32_e32 v172, v206
	v_mov_b32_e32 v173, v206
	v_mov_b32_e32 v170, v206
	v_mov_b32_e32 v171, v206
	v_mov_b32_e32 v168, v206
	v_mov_b32_e32 v169, v206
	v_mov_b32_e32 v166, v206
	v_mov_b32_e32 v167, v206
	v_mov_b32_e32 v164, v206
	v_mov_b32_e32 v165, v206
	v_mov_b32_e32 v162, v206
	v_mov_b32_e32 v163, v206
	v_mov_b32_e32 v160, v206
	v_mov_b32_e32 v161, v206
	v_mov_b32_e32 v158, v206
	v_mov_b32_e32 v159, v206
	s_nop 0

; __global__ void __launch_bounds__(NTHREADS, 2) mega_fwd(Args args) {
;     ...
;             if (has_next) { Wsb[(buf ^ 1) * 512 + (tid >> 5) * 32 + (tid & 31)] = wn; q0 = nq0; seg = nseg2; nadm = nnadm; buf ^= 1; }
;         }
.Lidx_wsb_done:
	s_branch .LBB0_647
	s_nop 0
	s_nop 0
	s_nop 0
	s_nop 0
	s_nop 0
	s_nop 0
	s_nop 0
	s_nop 0
	s_nop 0
	s_nop 0
	s_nop 0
	s_nop 0
	s_nop 0
	s_nop 0
	s_nop 0
